# prep touches the whole 4KiB page around its kernarg block (both directions) instead of a 2KiB forward window; rest as v40
# speedup vs baseline: 1.0054x; 1.0054x over previous
.Lprep_pf1:
	s_mov_b64 exec, s[20:21]
	v_cmp_gt_u32_e32 vcc, 0x100, v30
	s_and_saveexec_b64 s[20:21], vcc
	s_cbranch_execz .Lprep_pf2
	s_and_b32 s24, s0, 0xfffff000
	s_mov_b32 s25, s1
	v_lshlrev_b32_e32 v30, 4, v30
	global_load_dwordx4 v[32:35], v30, s[24:25]
